# k_point: role-1 KV0 global stores issued after the weight staging (converted data parked in spare VGPRs) so staging vmcnt waits no longer wait on store acks; explicit vmcnt(0) before them
# speedup vs baseline: 1.0048x; 1.0048x over previous
.LBB0_10:
	s_or_b64 exec, exec, s[8:9]
	s_waitcnt vmcnt(16)
	v_add_u32_e32 v70, v1, v107
	v_pk_add_f32 v[60:61], v[60:61], v[64:65]
	v_pk_add_f32 v[58:59], v[58:59], v[62:63]
	v_cvt_pk_f16_f32 v61, v60, v61
	v_cvt_pk_f16_f32 v60, v58, v59
	v_or_b32_e32 v58, v95, v70
	v_pk_add_f32 v[52:53], v[52:53], v[56:57]
	v_pk_add_f32 v[50:51], v[50:51], v[54:55]
	v_or_b32_e32 v1, v1, v102
	v_lshlrev_b32_e32 v71, 3, v102
	s_add_i32 s6, 0, 0x14300
	v_mul_u32_u24_e32 v58, 0x88, v58
	v_cvt_pk_f16_f32 v53, v52, v53
	v_cvt_pk_f16_f32 v52, v50, v51
	v_mul_u32_u24_e32 v1, 0x88, v1
	v_lshlrev_b32_e32 v50, 3, v95
	v_lshlrev_b32_e32 v93, 2, v95
	v_add3_u32 v58, s6, v71, v58
	v_add3_u32 v1, s6, v1, v50
	v_lshrrev_b32_e32 v50, 2, v102
	v_and_b32_e32 v87, 4, v93
	ds_write2_b64 v58, v[60:61], v[52:53] offset1:68
	v_or_b32_e32 v52, v87, v50
	v_or_b32_e32 v50, v93, v50
	s_movk_i32 s6, 0x2d00
	v_lshlrev_b32_e32 v95, 2, v102
	v_mul_u32_u24_e32 v50, 0x50, v50
	s_waitcnt lgkmcnt(0)
	s_barrier
	ds_read2_b64 v[54:57], v1 offset1:4
	ds_read2_b64 v[62:65], v1 offset0:8 offset1:12
	v_mad_u32_u24 v86, v104, s6, 0
	v_and_b32_e32 v51, 12, v95
	v_lshlrev_b32_e32 v88, 1, v50
	v_mul_u32_u24_e32 v91, 0x50, v52
	v_lshlrev_b32_e32 v92, 1, v51
	v_add_u32_e32 v121, v86, v88
	v_mul_u32_u24_e32 v1, 0x140, v104
	s_add_i32 s11, 0, 0x10e00
	v_lshl_add_u32 v96, v91, 1, v86
	v_add_u32_e32 v100, v121, v92
	v_cndmask_b32_e64 v122, 32, 16, s[4:5]
	v_cmp_gt_u32_e64 s[20:21], v122, v103
	s_waitcnt vmcnt(12)
	s_nop 1
	v_cndmask_b32_e64 v66, 0, v66, s[20:21]
	v_cndmask_b32_e64 v67, 0, v67, s[20:21]
	v_cndmask_b32_e64 v68, 0, v68, s[20:21]
	v_cndmask_b32_e64 v69, 0, v69, s[20:21]
	v_cvt_pk_f16_f32 v66, v66, v67
	v_cvt_pk_f16_f32 v67, v68, v69
	v_add3_u32 v1, s11, v1, v108
	v_add_u32_e32 v107, v96, v92
	v_add3_u32 v120, v86, v92, v88
	ds_read_b64_tr_b16 v[52:53], v100 offset:2560
	ds_read_b64_tr_b16 v[50:51], v120
	ds_read_b64_tr_b16 v[58:59], v120 offset:32
	ds_read_b64_tr_b16 v[68:69], v120 offset:5120
	ds_read_b64_tr_b16 v[70:71], v100 offset:7680
	ds_read_b128 v[72:75], v1
	ds_read_b128 v[76:79], v1 offset:64
	ds_read_b64_tr_b16 v[80:81], v120 offset:5152
	ds_read_b64_tr_b16 v[98:99], v120 offset:5248
	s_waitcnt vmcnt(15)
	ds_read_b64_tr_b16 v[108:109], v120 offset:64
	s_waitcnt vmcnt(12)
	ds_read_b64_tr_b16 v[112:113], v120 offset:5184
	s_waitcnt lgkmcnt(5)
	v_mfma_f32_16x16x32_f16 v[72:75], v[50:53], v[54:57], v[72:75]
	ds_read_b64_tr_b16 v[50:51], v107 offset:10240
	v_mov_b32_e32 v52, 0
	v_mov_b32_e32 v53, v52
	ds_read_b64_tr_b16 v[60:61], v100 offset:2592
	ds_read_b64_tr_b16 v[84:85], v100 offset:2688
	v_mfma_f32_16x16x32_f16 v[70:73], v[68:71], v[62:65], v[72:75]
	v_mov_b32_e32 v68, v52
	v_mov_b32_e32 v69, v52
	ds_read_b128 v[116:119], v1 offset:256
	s_waitcnt lgkmcnt(2)
	v_mfma_f32_16x16x32_f16 v[58:61], v[58:61], v[54:57], v[76:79]
	s_mov_b32 s7, 0x3fb504f3
	s_mov_b32 s9, 0x3ea7ba05
	s_mov_b32 s8, 0xbfba00e3
	v_mfma_f32_16x16x32_f16 v[70:73], v[50:53], v[66:69], v[70:73]
	ds_read_b64_tr_b16 v[82:83], v100 offset:7712
	ds_read_b64_tr_b16 v[110:111], v100 offset:2624
	ds_read_b64_tr_b16 v[50:51], v107 offset:10304
	v_mov_b32_e32 v76, v52
	v_mov_b32_e32 v77, v52
	s_waitcnt lgkmcnt(2)
	v_mfma_f32_16x16x32_f16 v[58:61], v[80:83], v[62:65], v[58:61]
	ds_read_b64_tr_b16 v[74:75], v107 offset:10272
	ds_read_b64_tr_b16 v[114:115], v100 offset:7744
	ds_read_b64_tr_b16 v[100:101], v100 offset:7808
	s_mov_b32 s6, 0x3f87dc22
	s_mov_b32 s10, 0xbe91a98e
	s_waitcnt lgkmcnt(2)
	v_mfma_f32_16x16x32_f16 v[74:77], v[74:77], v[66:69], v[58:61]
	s_nop 2
	ds_read_b128 v[58:61], v1 offset:128
	ds_read_b128 v[78:81], v1 offset:192
	v_or_b32_e32 v1, 48, v95
	v_lshlrev_b32_e32 v95, 1, v1
	v_add3_u32 v1, v86, v95, v88
	s_waitcnt lgkmcnt(1)
	v_mfma_f32_16x16x32_f16 v[58:61], v[108:111], v[54:57], v[58:61]
	ds_read_b64_tr_b16 v[108:109], v1
	ds_read_b64_tr_b16 v[82:83], v120 offset:128
	v_add_u32_e32 v120, v121, v95
	ds_read_b64_tr_b16 v[110:111], v120 offset:2560
	v_mfma_f32_16x16x32_f16 v[58:61], v[112:115], v[62:65], v[58:61]
	s_mov_b32 s12, 0x3e827906
	v_mfma_f32_16x16x32_f16 v[112:115], v[50:53], v[66:69], v[58:61]
	s_nop 5
	ds_read_b64_tr_b16 v[60:61], v120 offset:7680
	ds_read_b64_tr_b16 v[58:59], v1 offset:5120
	v_add_u32_e32 v1, v96, v95
	ds_read_b64_tr_b16 v[50:51], v1 offset:10240
	s_waitcnt lgkmcnt(3)
	v_mfma_f32_16x16x32_f16 v[78:81], v[108:111], v[54:57], v[78:81]
	s_waitcnt lgkmcnt(1)
	v_mfma_f32_16x16x32_f16 v[58:61], v[58:61], v[62:65], v[78:81]
	s_waitcnt lgkmcnt(0)
	v_mfma_f32_16x16x32_f16 v[58:61], v[50:53], v[66:69], v[58:61]
	ds_read_b64_tr_b16 v[50:51], v107 offset:10368
	v_mfma_f32_16x16x32_f16 v[54:57], v[82:85], v[54:57], v[116:119]
	v_mfma_f32_16x16x32_f16 v[54:57], v[98:101], v[62:65], v[54:57]
	s_waitcnt lgkmcnt(0)
	v_mfma_f32_16x16x32_f16 v[54:57], v[50:53], v[66:69], v[54:57]
	s_mov_b32 s24, 0x3fb504f3
	s_mov_b32 s26, 0x3ea7ba05
	s_mov_b32 s28, 0xbfb8aa3b
	s_mov_b32 s30, 0x3f87dc22
	s_mov_b32 s32, 0xbfba00e3
	s_mov_b32 s34, 0x3fb5f0e3
	s_mov_b32 s36, 0xbe91a98e
	s_mov_b32 s38, 0x3e827906
	v_mov_b32_e32 v152, s32
	v_mov_b32_e32 v153, s32
	v_pk_mul_f32 v[124:125], v[70:71], 0.5 op_sel_hi:[1,0]
	v_pk_mul_f32 v[138:139], v[72:73], 0.5 op_sel_hi:[1,0]
	v_and_b32_e32 v126, 0x7fffffff, v124
	v_and_b32_e32 v140, 0x7fffffff, v138
	v_and_b32_e32 v127, 0x7fffffff, v125
	v_and_b32_e32 v141, 0x7fffffff, v139
	v_pk_mul_f32 v[128:129], v[126:127], s[24:25] op_sel_hi:[1,0]
	v_pk_mul_f32 v[142:143], v[140:141], s[24:25] op_sel_hi:[1,0]
	v_pk_fma_f32 v[130:131], v[128:129], s[26:27], 1.0 op_sel_hi:[1,0,0]
	v_pk_fma_f32 v[144:145], v[142:143], s[26:27], 1.0 op_sel_hi:[1,0,0]
	v_pk_mul_f32 v[132:133], v[128:129], s[28:29] op_sel_hi:[1,0]
	v_pk_mul_f32 v[146:147], v[142:143], s[28:29] op_sel_hi:[1,0]
	v_rcp_f32_e32 v130, v130
	v_rcp_f32_e32 v144, v144
	v_rcp_f32_e32 v131, v131
	v_rcp_f32_e32 v145, v145
	v_pk_mul_f32 v[132:133], v[128:129], v[132:133]
	v_pk_mul_f32 v[146:147], v[142:143], v[146:147]
	v_exp_f32_e32 v132, v132
	v_exp_f32_e32 v146, v146
	v_exp_f32_e32 v133, v133
	v_exp_f32_e32 v147, v147
	v_pk_fma_f32 v[134:135], v[130:131], s[30:31], v[152:153] op_sel_hi:[1,0,0]
	v_pk_fma_f32 v[148:149], v[144:145], s[30:31], v[152:153] op_sel_hi:[1,0,0]
	v_pk_fma_f32 v[134:135], v[134:135], v[130:131], s[34:35] op_sel_hi:[1,1,0]
	v_pk_fma_f32 v[148:149], v[148:149], v[144:145], s[34:35] op_sel_hi:[1,1,0]
	v_pk_fma_f32 v[134:135], v[134:135], v[130:131], s[36:37] op_sel_hi:[1,1,0]
	v_pk_fma_f32 v[148:149], v[148:149], v[144:145], s[36:37] op_sel_hi:[1,1,0]
	v_pk_fma_f32 v[134:135], v[134:135], v[130:131], s[38:39] op_sel_hi:[1,1,0]
	v_pk_fma_f32 v[148:149], v[148:149], v[144:145], s[38:39] op_sel_hi:[1,1,0]
	v_pk_mul_f32 v[134:135], v[130:131], v[134:135]
	v_pk_mul_f32 v[148:149], v[144:145], v[148:149]
	v_pk_mul_f32 v[134:135], v[132:133], v[134:135]
	v_pk_mul_f32 v[148:149], v[146:147], v[148:149]
	v_pk_fma_f32 v[136:137], v[70:71], 0.5, v[126:127] op_sel_hi:[1,0,1]
	v_pk_fma_f32 v[150:151], v[72:73], 0.5, v[140:141] op_sel_hi:[1,0,1]
	v_pk_fma_f32 v[62:63], v[126:127], v[134:135], v[136:137] neg_lo:[1,0,0] neg_hi:[1,0,0]
	v_pk_fma_f32 v[64:65], v[140:141], v[148:149], v[150:151] neg_lo:[1,0,0] neg_hi:[1,0,0]
	v_pk_mul_f32 v[124:125], v[74:75], 0.5 op_sel_hi:[1,0]
	v_pk_mul_f32 v[138:139], v[76:77], 0.5 op_sel_hi:[1,0]
	v_and_b32_e32 v126, 0x7fffffff, v124
	v_and_b32_e32 v140, 0x7fffffff, v138
	v_and_b32_e32 v127, 0x7fffffff, v125
	v_and_b32_e32 v141, 0x7fffffff, v139
	v_pk_mul_f32 v[128:129], v[126:127], s[24:25] op_sel_hi:[1,0]
	v_pk_mul_f32 v[142:143], v[140:141], s[24:25] op_sel_hi:[1,0]
	v_pk_fma_f32 v[130:131], v[128:129], s[26:27], 1.0 op_sel_hi:[1,0,0]
	v_pk_fma_f32 v[144:145], v[142:143], s[26:27], 1.0 op_sel_hi:[1,0,0]
	v_pk_mul_f32 v[132:133], v[128:129], s[28:29] op_sel_hi:[1,0]
	v_pk_mul_f32 v[146:147], v[142:143], s[28:29] op_sel_hi:[1,0]
	v_rcp_f32_e32 v130, v130
	v_rcp_f32_e32 v144, v144
	v_rcp_f32_e32 v131, v131
	v_rcp_f32_e32 v145, v145
	v_pk_mul_f32 v[132:133], v[128:129], v[132:133]
	v_pk_mul_f32 v[146:147], v[142:143], v[146:147]
	v_exp_f32_e32 v132, v132
	v_exp_f32_e32 v146, v146
	v_exp_f32_e32 v133, v133
	v_exp_f32_e32 v147, v147
	v_pk_fma_f32 v[134:135], v[130:131], s[30:31], v[152:153] op_sel_hi:[1,0,0]
	v_pk_fma_f32 v[148:149], v[144:145], s[30:31], v[152:153] op_sel_hi:[1,0,0]
	v_pk_fma_f32 v[134:135], v[134:135], v[130:131], s[34:35] op_sel_hi:[1,1,0]
	v_pk_fma_f32 v[148:149], v[148:149], v[144:145], s[34:35] op_sel_hi:[1,1,0]
	v_pk_fma_f32 v[134:135], v[134:135], v[130:131], s[36:37] op_sel_hi:[1,1,0]
	v_pk_fma_f32 v[148:149], v[148:149], v[144:145], s[36:37] op_sel_hi:[1,1,0]
	v_pk_fma_f32 v[134:135], v[134:135], v[130:131], s[38:39] op_sel_hi:[1,1,0]
	v_pk_fma_f32 v[148:149], v[148:149], v[144:145], s[38:39] op_sel_hi:[1,1,0]
	v_pk_mul_f32 v[134:135], v[130:131], v[134:135]
	v_pk_mul_f32 v[148:149], v[144:145], v[148:149]
	v_pk_mul_f32 v[134:135], v[132:133], v[134:135]
	v_pk_mul_f32 v[148:149], v[146:147], v[148:149]
	v_pk_fma_f32 v[136:137], v[74:75], 0.5, v[126:127] op_sel_hi:[1,0,1]
	v_pk_fma_f32 v[150:151], v[76:77], 0.5, v[140:141] op_sel_hi:[1,0,1]
	v_pk_fma_f32 v[74:75], v[126:127], v[134:135], v[136:137] neg_lo:[1,0,0] neg_hi:[1,0,0]
	v_pk_fma_f32 v[76:77], v[140:141], v[148:149], v[150:151] neg_lo:[1,0,0] neg_hi:[1,0,0]
	v_pk_mul_f32 v[124:125], v[112:113], 0.5 op_sel_hi:[1,0]
	v_pk_mul_f32 v[138:139], v[114:115], 0.5 op_sel_hi:[1,0]
	v_and_b32_e32 v126, 0x7fffffff, v124
	v_and_b32_e32 v140, 0x7fffffff, v138
	v_and_b32_e32 v127, 0x7fffffff, v125
	v_and_b32_e32 v141, 0x7fffffff, v139
	v_pk_mul_f32 v[128:129], v[126:127], s[24:25] op_sel_hi:[1,0]
	v_pk_mul_f32 v[142:143], v[140:141], s[24:25] op_sel_hi:[1,0]
	v_pk_fma_f32 v[130:131], v[128:129], s[26:27], 1.0 op_sel_hi:[1,0,0]
	v_pk_fma_f32 v[144:145], v[142:143], s[26:27], 1.0 op_sel_hi:[1,0,0]
	v_pk_mul_f32 v[132:133], v[128:129], s[28:29] op_sel_hi:[1,0]
	v_pk_mul_f32 v[146:147], v[142:143], s[28:29] op_sel_hi:[1,0]
	v_rcp_f32_e32 v130, v130
	v_rcp_f32_e32 v144, v144
	v_rcp_f32_e32 v131, v131
	v_rcp_f32_e32 v145, v145
	v_pk_mul_f32 v[132:133], v[128:129], v[132:133]
	v_pk_mul_f32 v[146:147], v[142:143], v[146:147]
	v_exp_f32_e32 v132, v132
	v_exp_f32_e32 v146, v146
	v_exp_f32_e32 v133, v133
	v_exp_f32_e32 v147, v147
	v_pk_fma_f32 v[134:135], v[130:131], s[30:31], v[152:153] op_sel_hi:[1,0,0]
	v_pk_fma_f32 v[148:149], v[144:145], s[30:31], v[152:153] op_sel_hi:[1,0,0]
	v_pk_fma_f32 v[134:135], v[134:135], v[130:131], s[34:35] op_sel_hi:[1,1,0]
	v_pk_fma_f32 v[148:149], v[148:149], v[144:145], s[34:35] op_sel_hi:[1,1,0]
	v_pk_fma_f32 v[134:135], v[134:135], v[130:131], s[36:37] op_sel_hi:[1,1,0]
	v_pk_fma_f32 v[148:149], v[148:149], v[144:145], s[36:37] op_sel_hi:[1,1,0]
	v_pk_fma_f32 v[134:135], v[134:135], v[130:131], s[38:39] op_sel_hi:[1,1,0]
	v_pk_fma_f32 v[148:149], v[148:149], v[144:145], s[38:39] op_sel_hi:[1,1,0]
	v_pk_mul_f32 v[134:135], v[130:131], v[134:135]
	v_pk_mul_f32 v[148:149], v[144:145], v[148:149]
	v_pk_mul_f32 v[134:135], v[132:133], v[134:135]
	v_pk_mul_f32 v[148:149], v[146:147], v[148:149]
	v_pk_fma_f32 v[136:137], v[112:113], 0.5, v[126:127] op_sel_hi:[1,0,1]
	v_pk_fma_f32 v[150:151], v[114:115], 0.5, v[140:141] op_sel_hi:[1,0,1]
	v_pk_fma_f32 v[78:79], v[126:127], v[134:135], v[136:137] neg_lo:[1,0,0] neg_hi:[1,0,0]
	v_pk_fma_f32 v[80:81], v[140:141], v[148:149], v[150:151] neg_lo:[1,0,0] neg_hi:[1,0,0]
	v_pk_mul_f32 v[124:125], v[58:59], 0.5 op_sel_hi:[1,0]
	v_pk_mul_f32 v[138:139], v[60:61], 0.5 op_sel_hi:[1,0]
	v_and_b32_e32 v126, 0x7fffffff, v124
	v_and_b32_e32 v140, 0x7fffffff, v138
	v_and_b32_e32 v127, 0x7fffffff, v125
	v_and_b32_e32 v141, 0x7fffffff, v139
	v_pk_mul_f32 v[128:129], v[126:127], s[24:25] op_sel_hi:[1,0]
	v_pk_mul_f32 v[142:143], v[140:141], s[24:25] op_sel_hi:[1,0]
	v_pk_fma_f32 v[130:131], v[128:129], s[26:27], 1.0 op_sel_hi:[1,0,0]
	v_pk_fma_f32 v[144:145], v[142:143], s[26:27], 1.0 op_sel_hi:[1,0,0]
	v_pk_mul_f32 v[132:133], v[128:129], s[28:29] op_sel_hi:[1,0]
	v_pk_mul_f32 v[146:147], v[142:143], s[28:29] op_sel_hi:[1,0]
	v_rcp_f32_e32 v130, v130
	v_rcp_f32_e32 v144, v144
	v_rcp_f32_e32 v131, v131
	v_rcp_f32_e32 v145, v145
	v_pk_mul_f32 v[132:133], v[128:129], v[132:133]
	v_pk_mul_f32 v[146:147], v[142:143], v[146:147]
	v_exp_f32_e32 v132, v132
	v_exp_f32_e32 v146, v146
	v_exp_f32_e32 v133, v133
	v_exp_f32_e32 v147, v147
	v_pk_fma_f32 v[134:135], v[130:131], s[30:31], v[152:153] op_sel_hi:[1,0,0]
	v_pk_fma_f32 v[148:149], v[144:145], s[30:31], v[152:153] op_sel_hi:[1,0,0]
	v_pk_fma_f32 v[134:135], v[134:135], v[130:131], s[34:35] op_sel_hi:[1,1,0]
	v_pk_fma_f32 v[148:149], v[148:149], v[144:145], s[34:35] op_sel_hi:[1,1,0]
	v_pk_fma_f32 v[134:135], v[134:135], v[130:131], s[36:37] op_sel_hi:[1,1,0]
	v_pk_fma_f32 v[148:149], v[148:149], v[144:145], s[36:37] op_sel_hi:[1,1,0]
	v_pk_fma_f32 v[134:135], v[134:135], v[130:131], s[38:39] op_sel_hi:[1,1,0]
	v_pk_fma_f32 v[148:149], v[148:149], v[144:145], s[38:39] op_sel_hi:[1,1,0]
	v_pk_mul_f32 v[134:135], v[130:131], v[134:135]
	v_pk_mul_f32 v[148:149], v[144:145], v[148:149]
	v_pk_mul_f32 v[134:135], v[132:133], v[134:135]
	v_pk_mul_f32 v[148:149], v[146:147], v[148:149]
	v_pk_fma_f32 v[136:137], v[58:59], 0.5, v[126:127] op_sel_hi:[1,0,1]
	v_pk_fma_f32 v[150:151], v[60:61], 0.5, v[140:141] op_sel_hi:[1,0,1]
	v_pk_fma_f32 v[58:59], v[126:127], v[134:135], v[136:137] neg_lo:[1,0,0] neg_hi:[1,0,0]
	v_pk_fma_f32 v[60:61], v[140:141], v[148:149], v[150:151] neg_lo:[1,0,0] neg_hi:[1,0,0]
	v_pk_mul_f32 v[124:125], v[54:55], 0.5 op_sel_hi:[1,0]
	v_pk_mul_f32 v[138:139], v[56:57], 0.5 op_sel_hi:[1,0]
	v_and_b32_e32 v126, 0x7fffffff, v124
	v_and_b32_e32 v140, 0x7fffffff, v138
	v_and_b32_e32 v127, 0x7fffffff, v125
	v_and_b32_e32 v141, 0x7fffffff, v139
	v_pk_mul_f32 v[128:129], v[126:127], s[24:25] op_sel_hi:[1,0]
	v_pk_mul_f32 v[142:143], v[140:141], s[24:25] op_sel_hi:[1,0]
	v_pk_fma_f32 v[130:131], v[128:129], s[26:27], 1.0 op_sel_hi:[1,0,0]
	v_pk_fma_f32 v[144:145], v[142:143], s[26:27], 1.0 op_sel_hi:[1,0,0]
	v_pk_mul_f32 v[132:133], v[128:129], s[28:29] op_sel_hi:[1,0]
	v_pk_mul_f32 v[146:147], v[142:143], s[28:29] op_sel_hi:[1,0]
	v_rcp_f32_e32 v130, v130
	v_rcp_f32_e32 v144, v144
	v_rcp_f32_e32 v131, v131
	v_rcp_f32_e32 v145, v145
	v_pk_mul_f32 v[132:133], v[128:129], v[132:133]
	v_pk_mul_f32 v[146:147], v[142:143], v[146:147]
	v_exp_f32_e32 v132, v132
	v_exp_f32_e32 v146, v146
	v_exp_f32_e32 v133, v133
	v_exp_f32_e32 v147, v147
	v_pk_fma_f32 v[134:135], v[130:131], s[30:31], v[152:153] op_sel_hi:[1,0,0]
	v_pk_fma_f32 v[148:149], v[144:145], s[30:31], v[152:153] op_sel_hi:[1,0,0]
	v_pk_fma_f32 v[134:135], v[134:135], v[130:131], s[34:35] op_sel_hi:[1,1,0]
	v_pk_fma_f32 v[148:149], v[148:149], v[144:145], s[34:35] op_sel_hi:[1,1,0]
	v_pk_fma_f32 v[134:135], v[134:135], v[130:131], s[36:37] op_sel_hi:[1,1,0]
	v_pk_fma_f32 v[148:149], v[148:149], v[144:145], s[36:37] op_sel_hi:[1,1,0]
	v_pk_fma_f32 v[134:135], v[134:135], v[130:131], s[38:39] op_sel_hi:[1,1,0]
	v_pk_fma_f32 v[148:149], v[148:149], v[144:145], s[38:39] op_sel_hi:[1,1,0]
	v_pk_mul_f32 v[134:135], v[130:131], v[134:135]
	v_pk_mul_f32 v[148:149], v[144:145], v[148:149]
	v_pk_mul_f32 v[134:135], v[132:133], v[134:135]
	v_pk_mul_f32 v[148:149], v[146:147], v[148:149]
	v_pk_fma_f32 v[136:137], v[54:55], 0.5, v[126:127] op_sel_hi:[1,0,1]
	v_pk_fma_f32 v[150:151], v[56:57], 0.5, v[140:141] op_sel_hi:[1,0,1]
	v_pk_fma_f32 v[82:83], v[126:127], v[134:135], v[136:137] neg_lo:[1,0,0] neg_hi:[1,0,0]
	v_pk_fma_f32 v[84:85], v[140:141], v[148:149], v[150:151] neg_lo:[1,0,0] neg_hi:[1,0,0]
	v_cvt_pk_f16_f32 v73, v60, v61
	v_cvt_pk_f16_f32 v71, v80, v81
	v_cvt_pk_f16_f32 v70, v78, v79
	v_cvt_pk_f16_f32 v72, v58, v59
	v_cvt_pk_f16_f32 v69, v76, v77
	v_lshlrev_b32_e32 v50, 1, v93
	v_cvt_pk_f16_f32 v67, v64, v65
	v_cvt_pk_f16_f32 v66, v62, v63
	v_cvt_pk_f16_f32 v68, v74, v75
	s_and_saveexec_b64 s[6:7], s[4:5]
	s_xor_b64 s[6:7], exec, s[6:7]
	s_cbranch_execz .LBB0_14
	s_movk_i32 s10, 0x48
	v_mul_lo_u32 v0, v97, s10
	v_ashrrev_i32_e32 v1, 31, v0
	v_mov_b32_e32 v51, v52
	s_waitcnt lgkmcnt(0)
	v_lshl_add_u64 v[0:1], v[0:1], 1, s[64:65]
	v_lshl_add_u64 v[146:147], v[0:1], 0, v[50:51]
	v_cvt_pk_f16_f32 v137, v64, v65
	v_cvt_pk_f16_f32 v136, v62, v63
	v_cvt_pk_f16_f32 v139, v76, v77
	v_cvt_pk_f16_f32 v138, v74, v75
	v_cvt_pk_f16_f32 v141, v80, v81
	v_cvt_pk_f16_f32 v140, v78, v79
	v_cvt_pk_f16_f32 v143, v60, v61
	v_cvt_pk_f16_f32 v142, v58, v59
	v_cvt_pk_f16_f32 v145, v84, v85
	v_cvt_pk_f16_f32 v144, v82, v83

.LBB0_24:
	s_or_b64 exec, exec, s[0:1]
	s_waitcnt vmcnt(0)
	v_cmp_ne_u32_e64 s[0:1], 0, v104
	v_cmp_gt_u32_e64 s[8:9], 32, v103
	s_and_saveexec_b64 s[4:5], s[0:1]
	s_cbranch_execz .Lkv_skip
	global_store_dwordx2 v[146:147], v[136:137], off
	global_store_dwordx2 v[146:147], v[138:139], off offset:32
	global_store_dwordx2 v[146:147], v[140:141], off offset:64
	global_store_dwordx2 v[146:147], v[142:143], off offset:96
	s_and_b64 exec, exec, s[8:9]
	global_store_dwordx2 v[146:147], v[144:145], off offset:128
.Lkv_skip:
	s_or_b64 exec, exec, s[4:5]
	s_waitcnt lgkmcnt(0)
	s_barrier
	s_and_saveexec_b64 s[2:3], s[0:1]
	s_cbranch_execz .LBB0_26
	s_add_i32 s0, 0, 0x11300
	v_mul_u32_u24_e32 v0, 0xc00, v105
	v_add3_u32 v0, s0, v94, v0
	ds_read_b128 v[62:65], v0
	ds_read_b128 v[58:61], v0 offset:1024
	ds_read_b128 v[54:57], v0 offset:2048
	s_waitcnt lgkmcnt(2)
	v_mov_b32_e32 v52, v62
.LBB0_26:
	s_or_b64 exec, exec, s[2:3]
	v_or_b32_e32 v0, 2, v104
	s_movk_i32 s0, 0x2d00
	v_mad_u32_u24 v28, v0, s0, 0
	v_mul_u32_u24_e32 v0, 0x140, v0
	v_lshlrev_b32_e32 v1, 2, v93
	v_add_u32_e32 v30, v28, v88
	v_add3_u32 v29, s11, v0, v1
	v_add3_u32 v32, v28, v92, v88
	v_add_u32_e32 v33, v30, v92
	ds_read_b128 v[0:3], v29
	ds_read_b64_tr_b16 v[4:5], v32
	ds_read_b64_tr_b16 v[6:7], v33 offset:2560
	v_mov_b32_e32 v62, v52
	ds_read_b64_tr_b16 v[8:9], v32 offset:32
	v_lshl_add_u32 v31, v91, 1, v28
	s_waitcnt lgkmcnt(1)
	v_mfma_f32_16x16x32_f16 v[4:7], v[4:7], v[62:65], v[0:3]
	ds_read_b64_tr_b16 v[10:11], v33 offset:2592
	ds_read_b64_tr_b16 v[12:13], v32 offset:5120
	ds_read_b64_tr_b16 v[14:15], v33 offset:7680
	v_add_u32_e32 v34, v31, v92
	ds_read_b64_tr_b16 v[0:1], v34 offset:10240
	v_mov_b32_e32 v2, 0
	v_mov_b32_e32 v3, v2
	s_waitcnt lgkmcnt(1)
	v_mfma_f32_16x16x32_f16 v[4:7], v[12:15], v[58:61], v[4:7]
	ds_read_b64_tr_b16 v[12:13], v34 offset:10272
	ds_read_b128 v[16:19], v29 offset:64
	v_mov_b32_e32 v14, v2
	s_waitcnt lgkmcnt(2)
	v_mfma_f32_16x16x32_f16 v[4:7], v[0:3], v[54:57], v[4:7]
	ds_read_b64_tr_b16 v[20:21], v32 offset:5152
	ds_read_b64_tr_b16 v[22:23], v33 offset:7712
	v_mov_b32_e32 v15, v2
	s_waitcnt lgkmcnt(2)
	v_mfma_f32_16x16x32_f16 v[8:11], v[8:11], v[62:65], v[16:19]
	ds_read_b64_tr_b16 v[24:25], v32 offset:64
	v_add3_u32 v28, v28, v95, v88
	v_add_u32_e32 v30, v30, v95
	ds_read_b128 v[16:19], v29 offset:128
	s_waitcnt lgkmcnt(2)
	v_mfma_f32_16x16x32_f16 v[8:11], v[20:23], v[58:61], v[8:11]
	ds_read_b64_tr_b16 v[26:27], v33 offset:2624
	ds_read_b64_tr_b16 v[20:21], v32 offset:5184
	s_movk_i32 s2, 0x90
	v_mfma_f32_16x16x32_f16 v[8:11], v[12:15], v[54:57], v[8:11]
	ds_read_b64_tr_b16 v[22:23], v33 offset:7744
	ds_read_b64_tr_b16 v[0:1], v34 offset:10304
	v_mad_u32_u24 v35, v102, s2, v86
	s_waitcnt lgkmcnt(3)
	v_mfma_f32_16x16x32_f16 v[12:15], v[24:27], v[62:65], v[16:19]
	ds_read_b64_tr_b16 v[24:25], v28
	s_nop 1
	ds_read_b128 v[16:19], v29 offset:192
	v_add_u32_e32 v49, v35, v50
	s_waitcnt lgkmcnt(3)
	v_mfma_f32_16x16x32_f16 v[12:15], v[20:23], v[58:61], v[12:15]
	ds_read_b64_tr_b16 v[26:27], v30 offset:2560
	ds_read_b64_tr_b16 v[20:21], v28 offset:5120
	v_lshlrev_b32_e32 v48, 1, v87
	s_waitcnt lgkmcnt(4)
	v_mfma_f32_16x16x32_f16 v[12:15], v[0:3], v[54:57], v[12:15]
	ds_read_b64_tr_b16 v[22:23], v30 offset:7680
	v_add_u32_e32 v0, v31, v95
	ds_read_b64_tr_b16 v[0:1], v0 offset:10240
	s_waitcnt lgkmcnt(3)
	v_mfma_f32_16x16x32_f16 v[16:19], v[24:27], v[62:65], v[16:19]
	ds_read_b128 v[24:27], v29 offset:256
	ds_read_b64_tr_b16 v[28:29], v32 offset:128
	v_add_u32_e32 v36, v35, v48
	s_waitcnt lgkmcnt(3)
	v_mfma_f32_16x16x32_f16 v[16:19], v[20:23], v[58:61], v[16:19]
	ds_read_b64_tr_b16 v[30:31], v33 offset:2688
	ds_read_b64_tr_b16 v[20:21], v32 offset:5248
	v_add_u32_e32 v32, 0xb000, v49
	s_waitcnt lgkmcnt(4)
	v_mfma_f32_16x16x32_f16 v[16:19], v[0:3], v[54:57], v[16:19]
	ds_read_b64_tr_b16 v[22:23], v33 offset:7808
	ds_read_b64_tr_b16 v[0:1], v34 offset:10368
	v_add_u32_e32 v44, 0x80, v36
	v_add_u32_e32 v134, 0x180, v36
	s_waitcnt lgkmcnt(3)
	v_mfma_f32_16x16x32_f16 v[24:27], v[28:31], v[62:65], v[24:27]
	ds_read2_b64 v[28:31], v32 offset0:128 offset1:132
	ds_read2_b64 v[32:35], v32 offset0:136 offset1:140
	v_add_u32_e32 v40, 0xb800, v49
	s_waitcnt lgkmcnt(3)
	v_mfma_f32_16x16x32_f16 v[20:23], v[20:23], v[58:61], v[24:27]
	ds_read2_b64 v[36:39], v40 offset0:160 offset1:164
	v_cmp_gt_u32_e64 s[0:1], 32, v103
	v_cvt_pk_f16_f32 v11, v10, v11
	ds_read2st64_b64 v[126:129], v44 offset0:90 offset1:99
	s_waitcnt lgkmcnt(4)
	v_mfma_f32_16x16x32_f16 v[20:23], v[0:3], v[54:57], v[20:23]
	v_cvt_pk_f16_f32 v10, v8, v9
	v_cvt_pk_f16_f32 v9, v6, v7
	v_cvt_pk_f16_f32 v8, v4, v5
	ds_read2_b64 v[4:7], v40 offset0:168 offset1:172
	v_cvt_pk_f16_f32 v19, v18, v19
	s_nop 2
	v_cvt_pk_f16_f32 v0, v22, v23
	v_cvt_pk_f16_f32 v1, v20, v21
	v_cndmask_b32_e64 v21, 0, v0, s[0:1]
	v_add_u32_e32 v0, 0xc600, v49
	ds_read2_b64 v[40:43], v0 offset1:4
	s_waitcnt lgkmcnt(5)
	v_mfma_f32_16x16x32_f16 v[28:31], v[28:31], v[8:11], 0
	v_cndmask_b32_e64 v20, 0, v1, s[0:1]
	v_cvt_pk_f16_f32 v18, v16, v17
	v_cvt_pk_f16_f32 v17, v14, v15
	v_cvt_pk_f16_f32 v16, v12, v13
	ds_read2_b64 v[12:15], v0 offset0:8 offset1:12
	s_waitcnt lgkmcnt(3)
	v_mov_b32_e32 v0, v126
	v_mov_b32_e32 v1, v127
	ds_read2st64_b64 v[130:133], v134 offset0:94 offset1:103
	v_mfma_f32_16x16x32_f16 v[28:31], v[32:35], v[16:19], v[28:31]
	v_mov_b32_e32 v22, v2
	v_mov_b32_e32 v23, v2
	v_add_u32_e32 v24, 0xce00, v49
	ds_read2_b64 v[32:35], v24 offset0:32 offset1:36
	ds_read2_b64 v[52:55], v24 offset0:40 offset1:44
	v_mfma_f32_16x16x32_f16 v[28:31], v[0:3], v[20:23], v[28:31]
	v_or_b32_e32 v0, 64, v102
	v_min_u32_e32 v0, 0x47, v0
	v_mad_u32_u24 v49, v0, s2, v86
	v_add_u32_e32 v0, v49, v50
	v_add_u32_e32 v0, 0xb000, v0
	ds_read2_b64 v[56:59], v0 offset0:128 offset1:132
	ds_read2_b64 v[60:63], v0 offset0:136 offset1:140
	v_mfma_f32_16x16x32_f16 v[36:39], v[36:39], v[8:11], 0
	s_waitcnt lgkmcnt(4)
	v_mov_b32_e32 v0, v130
	v_mov_b32_e32 v1, v131
	s_movk_i32 s2, 0x48
	s_waitcnt lgkmcnt(7)
	v_mfma_f32_16x16x32_f16 v[4:7], v[4:7], v[16:19], v[36:39]
	v_mov_b32_e32 v51, v2
	v_mfma_f32_16x16x32_f16 v[24:27], v[0:3], v[20:23], v[4:7]
	s_waitcnt lgkmcnt(4)
	v_mov_b32_e32 v0, v128
	v_mov_b32_e32 v1, v129
	v_mfma_f32_16x16x32_f16 v[4:7], v[40:43], v[8:11], 0
	v_mfma_f32_16x16x32_f16 v[4:7], v[12:15], v[16:19], v[4:7]
	v_mfma_f32_16x16x32_f16 v[12:15], v[0:3], v[20:23], v[4:7]
	v_mov_b32_e32 v0, v132
	v_mov_b32_e32 v1, v133
	s_waitcnt lgkmcnt(3)
	v_mfma_f32_16x16x32_f16 v[4:7], v[32:35], v[8:11], 0
	s_waitcnt lgkmcnt(2)
	v_mfma_f32_16x16x32_f16 v[4:7], v[52:55], v[16:19], v[4:7]
	v_mfma_f32_16x16x32_f16 v[32:35], v[0:3], v[20:23], v[4:7]
	v_add_u32_e32 v0, v49, v48
	ds_read_b64 v[0:1], v0 offset:46208
	s_waitcnt lgkmcnt(2)
	v_mfma_f32_16x16x32_f16 v[4:7], v[56:59], v[8:11], 0
	v_mul_lo_u32 v8, v97, s2
	s_mov_b32 s2, 0x3e2e1a92
	v_ashrrev_i32_e32 v9, 31, v8
	s_waitcnt lgkmcnt(1)
	v_mfma_f32_16x16x32_f16 v[4:7], v[60:63], v[16:19], v[4:7]
	s_waitcnt lgkmcnt(0)
	v_mfma_f32_16x16x32_f16 v[4:7], v[0:3], v[20:23], v[4:7]
	v_mov_b32_e32 v0, s63
	v_mov_b32_e32 v1, s61
	v_cndmask_b32_e32 v1, v0, v1, vcc
	v_mov_b32_e32 v0, s62
	v_mov_b32_e32 v3, s60
	v_cndmask_b32_e32 v0, v0, v3, vcc
	v_mov_b32_e32 v2, v29
	v_mov_b32_e32 v3, v30
	v_pk_mul_f32 v[2:3], v[2:3], s[2:3] op_sel_hi:[1,0]
	v_lshl_add_u64 v[0:1], v[8:9], 1, v[0:1]
	v_fma_mixlo_f16 v8, v28, s2, 0
	v_cvt_pk_f16_f32 v3, v2, v3
	v_pack_b32_f16 v2, v8, v3
	v_fma_mixlo_f16 v8, v31, s2, 0
	v_lshl_add_u64 v[0:1], v[0:1], 0, v[50:51]
	v_alignbit_b32 v3, v8, v3, 16
	global_store_dwordx2 v[0:1], v[2:3], off
	v_mov_b32_e32 v2, v25
	v_mov_b32_e32 v3, v26
	v_pk_mul_f32 v[2:3], v[2:3], s[2:3] op_sel_hi:[1,0]
	v_fma_mixlo_f16 v8, v24, s2, 0
	v_cvt_pk_f16_f32 v3, v2, v3
	v_pack_b32_f16 v2, v8, v3
	v_fma_mixlo_f16 v8, v27, s2, 0
	v_alignbit_b32 v3, v8, v3, 16
	global_store_dwordx2 v[0:1], v[2:3], off offset:32
	v_mov_b32_e32 v2, v13
	v_mov_b32_e32 v3, v14
	v_pk_mul_f32 v[2:3], v[2:3], s[2:3] op_sel_hi:[1,0]
	v_fma_mixlo_f16 v8, v12, s2, 0
	v_cvt_pk_f16_f32 v3, v2, v3
	v_pack_b32_f16 v2, v8, v3
	v_fma_mixlo_f16 v8, v15, s2, 0
	v_alignbit_b32 v3, v8, v3, 16
	global_store_dwordx2 v[0:1], v[2:3], off offset:64
	v_mov_b32_e32 v2, v33
	v_mov_b32_e32 v3, v34
	v_pk_mul_f32 v[2:3], v[2:3], s[2:3] op_sel_hi:[1,0]
	v_fma_mixlo_f16 v8, v32, s2, 0
	v_cvt_pk_f16_f32 v3, v2, v3
	v_pack_b32_f16 v2, v8, v3
	v_fma_mixlo_f16 v8, v35, s2, 0
	v_alignbit_b32 v3, v8, v3, 16
	global_store_dwordx2 v[0:1], v[2:3], off offset:96
	s_and_saveexec_b64 s[4:5], s[0:1]
	s_cbranch_execz .LBB0_28
	v_mov_b32_e32 v2, v5
	v_mov_b32_e32 v3, v6
	v_pk_mul_f32 v[2:3], v[2:3], s[2:3] op_sel_hi:[1,0]
	v_fma_mixlo_f16 v4, v4, s2, 0
	v_cvt_pk_f16_f32 v3, v2, v3
	v_pack_b32_f16 v2, v4, v3
	v_fma_mixlo_f16 v4, v7, s2, 0
	v_alignbit_b32 v3, v4, v3, 16
	global_store_dwordx2 v[0:1], v[2:3], off offset:128
